# v18 + RWKV scan wave at s_setprio 3 (prep waves now have slack)
# speedup vs baseline: 1.0019x; 1.0019x over previous
.LBB0_1002:
	s_and_b64 vcc, exec, s[20:21]
	s_cbranch_vccz .LBB0_879
	s_setprio 3
	s_mov_b32 s8, 0x400001
	s_branch .LBB0_1005
